# best version plus 64-byte alignment of the five hot loop heads (code placement)
# speedup vs baseline: 1.0026x; 1.0026x over previous
.LBB1_6:
	v_mov_b32_e32 v2, 0x7f61b1e6
	v_mov_b32_e32 v195, 0x7f800000
	s_mov_b32 s10, -2
	v_mov_b32_e32 v114, v188
	s_mov_b32 s11, 32
	v_mov_b32_e32 v196, 0x7f800000
	v_mov_b32_e32 v197, 0x7f800000
	v_mov_b32_e32 v198, 0x7f800000
	v_mov_b32_e32 v3, v2
	v_mov_b32_e32 v4, v2
	v_mov_b32_e32 v5, v2
	v_mov_b32_e32 v6, v2
	v_mov_b32_e32 v7, v2
	v_mov_b32_e32 v8, v2
	v_mov_b32_e32 v9, v2
	v_mov_b32_e32 v10, v2
	v_mov_b32_e32 v11, v2
	v_mov_b32_e32 v12, v2
	v_mov_b32_e32 v13, v2
	v_mov_b32_e32 v14, v2
	v_mov_b32_e32 v15, v2
	v_mov_b32_e32 v16, v2
	v_mov_b32_e32 v17, v2
	.p2align 6

.LBB1_99:
	s_mov_b64 s[4:5], s[14:15]
	s_mov_b64 s[6:7], s[18:19]
	v_mov_b32_e32 v1, 0x22000
	s_barrier
	ds_read_b128 v[2:5], v1
	v_mov_b32_e32 v1, 0x22010
	ds_read_b128 v[6:9], v1
	s_mov_b32 s5, 0
	v_mov_b32_e32 v163, 0
	s_waitcnt lgkmcnt(1)
	v_readfirstlane_b32 s4, v2
	v_readfirstlane_b32 s8, v3
	s_lshl_b64 s[22:23], s[4:5], 10
	v_lshl_add_u64 v[66:67], s[6:7], 0, v[162:163]
	s_mov_b32 s9, s5
	v_readfirstlane_b32 s10, v4
	v_lshl_add_u64 v[2:3], v[66:67], 0, s[22:23]
	s_lshl_b64 s[6:7], s[8:9], 10
	s_mov_b32 s11, s5
	v_mov_b32_e32 v1, 0x22020
	v_readfirstlane_b32 s12, v5
	global_load_dwordx4 v[26:29], v[2:3], off
	v_lshl_add_u64 v[2:3], v[66:67], 0, s[6:7]
	s_lshl_b64 s[6:7], s[10:11], 10
	s_mov_b32 s13, s5
	ds_read_b128 v[34:37], v1
	global_load_dwordx4 v[18:21], v[2:3], off
	v_lshl_add_u64 v[2:3], v[66:67], 0, s[6:7]
	s_lshl_b64 s[6:7], s[12:13], 10
	s_waitcnt lgkmcnt(1)
	v_readfirstlane_b32 s4, v6
	global_load_dwordx4 v[10:13], v[2:3], off
	v_lshl_add_u64 v[2:3], v[66:67], 0, s[6:7]
	v_readfirstlane_b32 s6, v7
	s_lshl_b64 s[12:13], s[4:5], 10
	s_mov_b32 s7, s5
	v_readfirstlane_b32 s8, v8
	v_lshl_add_u64 v[6:7], v[66:67], 0, s[12:13]
	s_lshl_b64 s[6:7], s[6:7], 10
	v_mov_b32_e32 v1, 0x22030
	v_readfirstlane_b32 s10, v9
	global_load_dwordx4 v[30:33], v[6:7], off
	v_lshl_add_u64 v[6:7], v[66:67], 0, s[6:7]
	s_lshl_b64 s[6:7], s[8:9], 10
	ds_read_b128 v[38:41], v1
	global_load_dwordx4 v[14:17], v[6:7], off
	v_lshl_add_u64 v[6:7], v[66:67], 0, s[6:7]
	s_lshl_b64 s[6:7], s[10:11], 10
	s_waitcnt lgkmcnt(1)
	v_readfirstlane_b32 s4, v34
	v_lshl_add_u64 v[22:23], v[66:67], 0, s[6:7]
	v_readfirstlane_b32 s6, v35
	s_lshl_b64 s[12:13], s[4:5], 10
	s_mov_b32 s7, s5
	v_readfirstlane_b32 s8, v36
	v_lshl_add_u64 v[34:35], v[66:67], 0, s[12:13]
	s_lshl_b64 s[6:7], s[6:7], 10
	v_readfirstlane_b32 s10, v37
	global_load_dwordx4 v[58:61], v[34:35], off
	v_lshl_add_u64 v[34:35], v[66:67], 0, s[6:7]
	s_lshl_b64 s[6:7], s[8:9], 10
	global_load_dwordx4 v[54:57], v[34:35], off
	v_lshl_add_u64 v[34:35], v[66:67], 0, s[6:7]
	s_lshl_b64 s[6:7], s[10:11], 10
	s_waitcnt lgkmcnt(0)
	v_readfirstlane_b32 s4, v38
	global_load_dwordx4 v[46:49], v[34:35], off
	v_lshl_add_u64 v[34:35], v[66:67], 0, s[6:7]
	v_readfirstlane_b32 s6, v39
	s_lshl_b64 s[12:13], s[4:5], 10
	s_mov_b32 s7, s5
	v_readfirstlane_b32 s8, v40
	v_lshl_add_u64 v[38:39], v[66:67], 0, s[12:13]
	s_lshl_b64 s[6:7], s[6:7], 10
	v_readfirstlane_b32 s10, v41
	global_load_dwordx4 v[62:65], v[38:39], off
	v_lshl_add_u64 v[38:39], v[66:67], 0, s[6:7]
	s_lshl_b64 s[6:7], s[8:9], 10
	global_load_dwordx4 v[50:53], v[38:39], off
	v_lshl_add_u64 v[38:39], v[66:67], 0, s[6:7]
	s_lshl_b64 s[6:7], s[10:11], 10
	global_load_dwordx4 v[42:45], v[38:39], off
	v_lshl_add_u64 v[38:39], v[66:67], 0, s[6:7]
	s_mov_b64 s[6:7], s[14:15]
	s_mov_b64 s[8:9], s[18:19]
	v_mov_b32_e32 v1, 0x22040
	global_load_dwordx4 v[2:5], v[2:3], off
	s_mov_b32 s13, s5
	global_load_dwordx4 v[6:9], v[6:7], off
	s_mov_b32 s3, 0x22080
	global_load_dwordx4 v[22:25], v[22:23], off
	s_mov_b32 s99, 0
	global_load_dwordx4 v[34:37], v[34:35], off
	s_mov_b32 vcc_lo, s98
	global_load_dwordx4 v[38:41], v[38:39], off
	s_barrier
	ds_read_b128 v[66:69], v1
	v_mov_b32_e32 v1, 0x22050
	ds_read_b128 v[82:85], v1
	v_lshl_add_u64 v[114:115], s[8:9], 0, v[162:163]
	s_mov_b32 s7, s5
	s_waitcnt lgkmcnt(1)
	v_readfirstlane_b32 s4, v66
	v_readfirstlane_b32 s6, v67
	s_lshl_b64 s[22:23], s[4:5], 10
	v_readfirstlane_b32 s10, v68
	v_lshl_add_u64 v[66:67], v[114:115], 0, s[22:23]
	s_lshl_b64 s[6:7], s[6:7], 10
	v_mov_b32_e32 v1, 0x22060
	v_readfirstlane_b32 s12, v69
	global_load_dwordx4 v[78:81], v[66:67], off
	v_lshl_add_u64 v[66:67], v[114:115], 0, s[6:7]
	s_lshl_b64 s[6:7], s[10:11], 10
	ds_read_b128 v[94:97], v1
	global_load_dwordx4 v[74:77], v[66:67], off
	v_lshl_add_u64 v[66:67], v[114:115], 0, s[6:7]
	s_lshl_b64 s[6:7], s[12:13], 10
	s_waitcnt lgkmcnt(1)
	v_readfirstlane_b32 s4, v82
	global_load_dwordx4 v[70:73], v[66:67], off
	v_lshl_add_u64 v[66:67], v[114:115], 0, s[6:7]
	v_readfirstlane_b32 s6, v83
	s_lshl_b64 s[12:13], s[4:5], 10
	s_mov_b32 s7, s5
	v_readfirstlane_b32 s8, v84
	v_lshl_add_u64 v[82:83], v[114:115], 0, s[12:13]
	s_lshl_b64 s[6:7], s[6:7], 10
	s_mov_b32 s9, s5
	v_mov_b32_e32 v1, 0x22070
	v_readfirstlane_b32 s10, v85
	global_load_dwordx4 v[118:121], v[82:83], off
	v_lshl_add_u64 v[82:83], v[114:115], 0, s[6:7]
	s_lshl_b64 s[6:7], s[8:9], 10
	ds_read_b128 v[106:109], v1
	global_load_dwordx4 v[86:89], v[82:83], off
	v_lshl_add_u64 v[82:83], v[114:115], 0, s[6:7]
	s_lshl_b64 s[6:7], s[10:11], 10
	s_waitcnt lgkmcnt(1)
	v_readfirstlane_b32 s4, v94
	v_lshl_add_u64 v[90:91], v[114:115], 0, s[6:7]
	v_readfirstlane_b32 s6, v95
	s_lshl_b64 s[12:13], s[4:5], 10
	s_mov_b32 s7, s5
	v_readfirstlane_b32 s8, v96
	v_lshl_add_u64 v[94:95], v[114:115], 0, s[12:13]
	s_lshl_b64 s[6:7], s[6:7], 10
	v_readfirstlane_b32 s10, v97
	global_load_dwordx4 v[126:129], v[94:95], off
	v_lshl_add_u64 v[94:95], v[114:115], 0, s[6:7]
	s_lshl_b64 s[6:7], s[8:9], 10
	global_load_dwordx4 v[102:105], v[94:95], off
	v_lshl_add_u64 v[94:95], v[114:115], 0, s[6:7]
	s_lshl_b64 s[6:7], s[10:11], 10
	s_waitcnt lgkmcnt(0)
	v_readfirstlane_b32 s4, v106
	global_load_dwordx4 v[98:101], v[94:95], off
	v_lshl_add_u64 v[94:95], v[114:115], 0, s[6:7]
	v_readfirstlane_b32 s6, v107
	s_lshl_b64 s[12:13], s[4:5], 10
	s_mov_b32 s7, s5
	v_readfirstlane_b32 s8, v108
	v_lshl_add_u64 v[106:107], v[114:115], 0, s[12:13]
	s_lshl_b64 s[6:7], s[6:7], 10
	v_readfirstlane_b32 s10, v109
	global_load_dwordx4 v[122:125], v[106:107], off
	v_lshl_add_u64 v[106:107], v[114:115], 0, s[6:7]
	s_lshl_b64 s[6:7], s[8:9], 10
	global_load_dwordx4 v[110:113], v[106:107], off
	v_lshl_add_u64 v[106:107], v[114:115], 0, s[6:7]
	s_lshl_b64 s[6:7], s[10:11], 10
	v_lshl_add_u64 v[114:115], v[114:115], 0, s[6:7]
	global_load_dwordx4 v[66:69], v[66:67], off
	s_mov_b32 vcc_hi, 0
	global_load_dwordx4 v[82:85], v[82:83], off
	s_nop 0
	global_load_dwordx4 v[90:93], v[90:91], off
	s_nop 0
	global_load_dwordx4 v[94:97], v[94:95], off
	s_nop 0
	global_load_dwordx4 v[106:109], v[106:107], off
	s_nop 0
	global_load_dwordx4 v[114:117], v[114:115], off
	s_barrier
	.p2align 6

.LBB1_106:
	s_xor_b64 s[6:7], s[8:9], -1
	s_lshl_b32 s99, s3, 4
	s_lshl_b32 vcc_lo, s3, 12
	s_mov_b32 vcc_hi, -2
	s_mov_b32 s3, 0x22000
	.p2align 6

.LBB1_144:
	s_xor_b64 s[42:43], s[8:9], -1
	s_mov_b32 s41, 1
	s_mov_b64 s[8:9], 0
	s_and_b64 vcc, exec, s[42:43]
	s_barrier
	s_cbranch_vccnz .LBB1_148
	.p2align 6

.LBB1_188:
	s_mov_b32 s10, -2
	v_mov_b64_e32 v[66:67], v[64:65]
	s_movk_i32 s11, 0x1800
	.p2align 6
